# attention K/V sharing with a third barrier before the PV loop (V' DMA may stay in flight through the next unit's K loop and softmax; counted wait vmcnt 12)
# speedup vs baseline: 1.0136x; 1.0092x over previous
.LBB0_451:
	s_mov_b32 m0, s25
	s_nop 0
	ds_read_b128 v[50:53], v221 offset:45056
	ds_read_b128 v[66:69], v222 offset:45056
	s_waitcnt lgkmcnt(0)
	v_mfma_f32_32x32x16_bf16 v[50:65], v[50:53], v[158:161], 0
	v_mfma_f32_32x32x16_bf16 v[50:65], v[66:69], v[154:157], v[50:65]
	ds_read_b128 v[66:69], v223 offset:45056
	s_waitcnt lgkmcnt(0)
	v_mfma_f32_32x32x16_bf16 v[50:65], v[66:69], v[150:153], v[50:65]
	ds_read_b128 v[66:69], v224 offset:45056
	s_waitcnt lgkmcnt(0)
	s_waitcnt lgkmcnt(0)
	v_mfma_f32_32x32x16_bf16 v[50:65], v[66:69], v[146:149], v[50:65]
	ds_read_b128 v[66:69], v221 offset:49152
	ds_read_b128 v[82:85], v222 offset:49152
	s_waitcnt lgkmcnt(0)
	v_mfma_f32_32x32x16_bf16 v[66:81], v[66:69], v[158:161], 0
	v_mfma_f32_32x32x16_bf16 v[66:81], v[82:85], v[154:157], v[66:81]
	ds_read_b128 v[82:85], v223 offset:49152
	s_waitcnt lgkmcnt(0)
	v_mfma_f32_32x32x16_bf16 v[66:81], v[82:85], v[150:153], v[66:81]
	ds_read_b128 v[82:85], v224 offset:49152
	s_waitcnt lgkmcnt(0)
	s_waitcnt lgkmcnt(0)
	v_mfma_f32_32x32x16_bf16 v[66:81], v[82:85], v[146:149], v[66:81]
	s_barrier
	s_add_i32 s38, s53, 1
	s_cmp_lt_i32 s38, s0
	s_cselect_b64 s[96:97], -1, 0
	s_cmp_ge_i32 s38, s0
	s_mov_b32 s39, s86
	s_mov_b32 s40, s88
	s_mov_b32 s47, s81
	s_mov_b32 s41, s33
	s_mov_b32 s80, s42
	s_mov_b32 s48, s82
	v_mov_b32_e32 v183, v180
	v_mov_b32_e32 v190, v178
	v_mov_b32_e32 v187, v182
	s_cbranch_scc1 .LBB0_466
	v_readlane_b32 s40, v254, 8
	v_readlane_b32 s41, v254, 9
	s_mov_b64 s[4:5], -1
	s_and_b64 vcc, exec, s[40:41]
	s_cbranch_vccz .LBB0_454
	s_mul_i32 s4, s38, s74
	v_readlane_b32 s40, v254, 19
	v_readlane_b32 s41, v254, 20
	s_add_i32 s39, s4, s40
	s_mov_b64 s[4:5], 0

.LBB0_471:
	v_max_f32_e32 v33, v18, v18
	v_max_f32_e32 v66, v97, v97
	v_max_f32_e32 v33, v66, v33
	v_max_f32_e32 v66, v20, v20
	v_max_f32_e32 v67, v19, v19
	v_max_f32_e32 v66, v67, v66
	s_mov_b32 s4, 0xff800000
	v_max3_f32 v33, v33, s4, v66
	v_max_f32_e32 v66, v22, v22
	v_max_f32_e32 v67, v21, v21
	v_max_f32_e32 v66, v67, v66
	v_max_f32_e32 v67, v24, v24
	v_max_f32_e32 v68, v23, v23
	v_max_f32_e32 v67, v68, v67
	v_max3_f32 v33, v33, v66, v67
	v_max_f32_e32 v66, v26, v26
	v_max_f32_e32 v67, v25, v25
	v_max_f32_e32 v66, v67, v66
	v_max_f32_e32 v67, v28, v28
	v_max_f32_e32 v68, v27, v27
	v_max_f32_e32 v67, v68, v67
	v_max3_f32 v33, v33, v66, v67
	v_max_f32_e32 v66, v31, v31
	v_max_f32_e32 v67, v29, v29
	v_max_f32_e32 v66, v67, v66
	v_max_f32_e32 v67, v30, v30
	v_max_f32_e32 v68, v32, v32
	v_max_f32_e32 v67, v68, v67
	v_max3_f32 v33, v33, v66, v67
	v_max_f32_e32 v66, v3, v3
	v_max_f32_e32 v67, v2, v2
	v_max_f32_e32 v66, v67, v66
	v_max_f32_e32 v67, v5, v5
	v_max_f32_e32 v68, v4, v4
	v_max_f32_e32 v67, v68, v67
	v_max3_f32 v33, v33, v66, v67
	v_max_f32_e32 v66, v7, v7
	v_max_f32_e32 v67, v6, v6
	v_max_f32_e32 v66, v67, v66
	v_max_f32_e32 v67, v9, v9
	v_max_f32_e32 v68, v8, v8
	v_max_f32_e32 v67, v68, v67
	v_max3_f32 v33, v33, v66, v67
	v_max_f32_e32 v66, v11, v11
	v_max_f32_e32 v67, v10, v10
	v_max_f32_e32 v66, v67, v66
	v_max_f32_e32 v67, v13, v13
	v_max_f32_e32 v68, v12, v12
	v_max_f32_e32 v67, v68, v67
	v_max3_f32 v33, v33, v66, v67
	v_max_f32_e32 v66, v15, v15
	v_max_f32_e32 v67, v14, v14
	v_max_f32_e32 v66, v67, v66
	v_max_f32_e32 v67, v17, v17
	v_max_f32_e32 v68, v16, v16
	v_max_f32_e32 v67, v68, v67
	v_max3_f32 v33, v33, v66, v67
	v_max_f32_e32 v66, v35, v35
	v_max_f32_e32 v67, v34, v34
	v_max_f32_e32 v66, v67, v66
	v_max_f32_e32 v67, v37, v37
	v_max_f32_e32 v68, v36, v36
	v_max_f32_e32 v67, v68, v67
	v_max3_f32 v33, v33, v66, v67
	v_max_f32_e32 v66, v39, v39
	v_max_f32_e32 v67, v38, v38
	v_max_f32_e32 v66, v67, v66
	v_max_f32_e32 v67, v41, v41
	v_max_f32_e32 v68, v40, v40
	v_max_f32_e32 v67, v68, v67
	v_max3_f32 v33, v33, v66, v67
	v_max_f32_e32 v66, v43, v43
	v_max_f32_e32 v67, v42, v42
	v_max_f32_e32 v66, v67, v66
	v_max_f32_e32 v67, v45, v45
	v_max_f32_e32 v68, v44, v44
	v_max_f32_e32 v67, v68, v67
	v_max3_f32 v33, v33, v66, v67
	v_max_f32_e32 v66, v47, v47
	v_max_f32_e32 v67, v46, v46
	v_max_f32_e32 v66, v67, v66
	v_max_f32_e32 v67, v49, v49
	v_max_f32_e32 v68, v48, v48
	v_max_f32_e32 v67, v68, v67
	v_max3_f32 v33, v33, v66, v67
	v_max_f32_e32 v66, v51, v51
	v_max_f32_e32 v67, v50, v50
	v_max_f32_e32 v66, v67, v66
	v_max_f32_e32 v67, v53, v53
	v_max_f32_e32 v68, v52, v52
	v_max_f32_e32 v67, v68, v67
	v_max3_f32 v33, v33, v66, v67
	v_max_f32_e32 v66, v55, v55
	v_max_f32_e32 v67, v54, v54
	v_max_f32_e32 v66, v67, v66
	v_max_f32_e32 v67, v57, v57
	v_max_f32_e32 v68, v56, v56
	v_max_f32_e32 v67, v68, v67
	v_max3_f32 v33, v33, v66, v67
	v_max_f32_e32 v66, v59, v59
	v_max_f32_e32 v67, v58, v58
	v_max_f32_e32 v66, v67, v66
	v_max_f32_e32 v67, v61, v61
	v_max_f32_e32 v68, v60, v60
	v_max_f32_e32 v67, v68, v67
	v_max3_f32 v33, v33, v66, v67
	v_max_f32_e32 v66, v63, v63
	v_max_f32_e32 v67, v62, v62
	v_max_f32_e32 v66, v67, v66
	v_max_f32_e32 v67, v65, v65
	v_max_f32_e32 v68, v64, v64
	v_max_f32_e32 v67, v68, v67
	v_max3_f32 v33, v33, v66, v67
	v_max_f32_e32 v66, v83, v83
	v_max_f32_e32 v67, v82, v82
	v_max_f32_e32 v66, v67, v66
	v_max_f32_e32 v67, v85, v85
	v_max_f32_e32 v68, v84, v84
	v_max_f32_e32 v67, v68, v67
	v_max3_f32 v33, v33, v66, v67
	v_max_f32_e32 v66, v87, v87
	v_max_f32_e32 v67, v86, v86
	v_max_f32_e32 v66, v67, v66
	v_max_f32_e32 v67, v89, v89
	v_max_f32_e32 v68, v88, v88
	v_max_f32_e32 v67, v68, v67
	v_max3_f32 v33, v33, v66, v67
	v_max_f32_e32 v66, v91, v91
	v_max_f32_e32 v67, v90, v90
	v_max_f32_e32 v66, v67, v66
	v_max_f32_e32 v67, v93, v93
	v_max_f32_e32 v68, v92, v92
	v_max_f32_e32 v67, v68, v67
	v_cndmask_b32_e64 v70, v81, v226, s[78:79]
	v_max3_f32 v33, v33, v66, v67
	v_max_f32_e32 v66, v95, v95
	v_max_f32_e32 v67, v94, v94
	v_max_f32_e32 v66, v67, v66
	v_max_f32_e32 v67, v70, v70
	v_max_f32_e32 v68, v96, v96
	v_max_f32_e32 v67, v68, v67
	v_max3_f32 v33, v33, v66, v67
	v_and_b32_e32 v67, 64, v209
	v_xor_b32_e32 v66, 32, v209
	v_add_u32_e32 v67, 64, v67
	v_cmp_lt_i32_e32 vcc, v66, v67
	s_nop 1
	v_cndmask_b32_e32 v66, v209, v66, vcc
	v_lshlrev_b32_e32 v118, 2, v66
	ds_bpermute_b32 v66, v118, v33
	s_waitcnt lgkmcnt(0)
	v_max_f32_e32 v66, v66, v66
	v_max_f32_e32 v66, v33, v66
	v_sub_f32_e32 v33, v97, v66
	v_exp_f32_e32 v33, v33
	v_sub_f32_e32 v18, v18, v66
	v_exp_f32_e32 v18, v18
	v_sub_f32_e32 v19, v19, v66
	v_exp_f32_e32 v19, v19
	v_sub_f32_e32 v20, v20, v66
	v_exp_f32_e32 v20, v20
	v_sub_f32_e32 v21, v21, v66
	v_add_f32_e32 v67, 0, v33
	v_exp_f32_e32 v21, v21
	v_sub_f32_e32 v22, v22, v66
	v_add_f32_e32 v67, v18, v67
	v_exp_f32_e32 v22, v22
	v_sub_f32_e32 v23, v23, v66
	v_add_f32_e32 v67, v19, v67
	v_exp_f32_e32 v23, v23
	v_sub_f32_e32 v24, v24, v66
	v_add_f32_e32 v67, v20, v67
	v_exp_f32_e32 v24, v24
	v_sub_f32_e32 v25, v25, v66
	v_add_f32_e32 v67, v21, v67
	v_exp_f32_e32 v119, v25
	v_sub_f32_e32 v25, v26, v66
	v_add_f32_e32 v67, v22, v67
	v_exp_f32_e32 v120, v25
	v_sub_f32_e32 v25, v27, v66
	v_add_f32_e32 v67, v23, v67
	v_exp_f32_e32 v121, v25
	v_sub_f32_e32 v26, v28, v66
	v_add_f32_e32 v25, v24, v67
	v_exp_f32_e32 v122, v26
	v_sub_f32_e32 v26, v29, v66
	v_add_f32_e32 v25, v119, v25
	v_exp_f32_e32 v123, v26
	v_sub_f32_e32 v26, v31, v66
	v_add_f32_e32 v25, v120, v25
	v_exp_f32_e32 v124, v26
	v_sub_f32_e32 v26, v32, v66
	v_add_f32_e32 v25, v121, v25
	v_exp_f32_e32 v125, v26
	v_sub_f32_e32 v26, v30, v66
	v_add_f32_e32 v25, v122, v25
	v_exp_f32_e32 v126, v26
	v_sub_f32_e32 v2, v2, v66
	v_add_f32_e32 v25, v123, v25
	v_exp_f32_e32 v103, v2
	v_sub_f32_e32 v2, v3, v66
	v_add_f32_e32 v25, v124, v25
	v_exp_f32_e32 v106, v2
	v_sub_f32_e32 v2, v4, v66
	v_add_f32_e32 v25, v125, v25
	v_exp_f32_e32 v107, v2
	v_sub_f32_e32 v3, v5, v66
	v_add_f32_e32 v2, v126, v25
	v_exp_f32_e32 v110, v3
	v_sub_f32_e32 v3, v6, v66
	v_add_f32_e32 v2, v103, v2
	v_exp_f32_e32 v111, v3
	v_sub_f32_e32 v3, v7, v66
	v_add_f32_e32 v2, v106, v2
	v_exp_f32_e32 v114, v3
	v_sub_f32_e32 v3, v8, v66
	v_add_f32_e32 v2, v107, v2
	v_exp_f32_e32 v115, v3
	v_sub_f32_e32 v3, v9, v66
	v_add_f32_e32 v2, v110, v2
	v_exp_f32_e32 v117, v3
	v_sub_f32_e32 v3, v10, v66
	v_add_f32_e32 v2, v111, v2
	v_exp_f32_e32 v102, v3
	v_sub_f32_e32 v3, v11, v66
	v_add_f32_e32 v2, v114, v2
	v_exp_f32_e32 v104, v3
	v_sub_f32_e32 v3, v12, v66
	v_add_f32_e32 v2, v115, v2
	v_exp_f32_e32 v105, v3
	v_sub_f32_e32 v3, v13, v66
	v_add_f32_e32 v2, v117, v2
	v_exp_f32_e32 v108, v3
	v_sub_f32_e32 v3, v14, v66
	v_add_f32_e32 v2, v102, v2
	v_exp_f32_e32 v109, v3
	v_sub_f32_e32 v3, v15, v66
	v_add_f32_e32 v2, v104, v2
	v_exp_f32_e32 v112, v3
	v_sub_f32_e32 v3, v16, v66
	v_add_f32_e32 v2, v105, v2
	v_exp_f32_e32 v113, v3
	v_sub_f32_e32 v3, v17, v66
	v_add_f32_e32 v2, v108, v2
	v_exp_f32_e32 v116, v3
	v_sub_f32_e32 v3, v34, v66
	v_add_f32_e32 v2, v109, v2
	v_exp_f32_e32 v72, v3
	v_sub_f32_e32 v3, v35, v66
	v_add_f32_e32 v2, v112, v2
	v_exp_f32_e32 v75, v3
	v_sub_f32_e32 v3, v36, v66
	v_add_f32_e32 v2, v113, v2
	v_exp_f32_e32 v76, v3
	v_sub_f32_e32 v3, v37, v66
	v_add_f32_e32 v2, v116, v2
	v_exp_f32_e32 v79, v3
	v_sub_f32_e32 v3, v38, v66
	v_add_f32_e32 v2, v72, v2
	v_exp_f32_e32 v80, v3
	v_sub_f32_e32 v3, v39, v66
	v_add_f32_e32 v2, v75, v2
	v_exp_f32_e32 v98, v3
	v_sub_f32_e32 v3, v40, v66
	v_add_f32_e32 v2, v76, v2
	v_exp_f32_e32 v99, v3
	v_sub_f32_e32 v3, v41, v66
	v_add_f32_e32 v2, v79, v2
	v_exp_f32_e32 v101, v3
	v_sub_f32_e32 v3, v42, v66
	v_add_f32_e32 v2, v80, v2
	v_exp_f32_e32 v71, v3
	v_sub_f32_e32 v3, v43, v66
	v_add_f32_e32 v2, v98, v2
	v_exp_f32_e32 v73, v3
	v_sub_f32_e32 v3, v44, v66
	v_add_f32_e32 v2, v99, v2
	v_exp_f32_e32 v74, v3
	v_sub_f32_e32 v3, v45, v66
	v_add_f32_e32 v2, v101, v2
	v_exp_f32_e32 v77, v3
	v_sub_f32_e32 v3, v46, v66
	v_add_f32_e32 v2, v71, v2
	v_exp_f32_e32 v78, v3
	v_sub_f32_e32 v3, v47, v66
	v_add_f32_e32 v2, v73, v2
	v_exp_f32_e32 v81, v3
	v_sub_f32_e32 v3, v48, v66
	v_add_f32_e32 v2, v74, v2
	v_exp_f32_e32 v97, v3
	v_sub_f32_e32 v3, v49, v66
	v_add_f32_e32 v2, v77, v2
	v_exp_f32_e32 v100, v3
	v_sub_f32_e32 v3, v50, v66
	v_add_f32_e32 v2, v78, v2
	v_exp_f32_e32 v41, v3
	v_sub_f32_e32 v3, v51, v66
	v_add_f32_e32 v2, v81, v2
	v_exp_f32_e32 v46, v3
	v_sub_f32_e32 v3, v52, v66
	v_add_f32_e32 v2, v97, v2
	v_exp_f32_e32 v47, v3
	v_sub_f32_e32 v3, v53, v66
	v_add_f32_e32 v2, v100, v2
	v_exp_f32_e32 v53, v3
	v_sub_f32_e32 v3, v54, v66
	v_add_f32_e32 v2, v41, v2
	v_exp_f32_e32 v54, v3
	v_sub_f32_e32 v3, v55, v66
	v_add_f32_e32 v2, v46, v2
	v_exp_f32_e32 v67, v3
	v_sub_f32_e32 v3, v56, v66
	v_add_f32_e32 v2, v47, v2
	v_exp_f32_e32 v68, v3
	v_sub_f32_e32 v3, v57, v66
	v_add_f32_e32 v2, v53, v2
	v_exp_f32_e32 v69, v3
	v_sub_f32_e32 v3, v58, v66
	v_add_f32_e32 v2, v54, v2
	v_exp_f32_e32 v38, v3
	v_sub_f32_e32 v3, v59, v66
	v_add_f32_e32 v2, v67, v2
	v_exp_f32_e32 v44, v3
	v_sub_f32_e32 v3, v60, v66
	v_add_f32_e32 v2, v68, v2
	v_exp_f32_e32 v45, v3
	v_sub_f32_e32 v3, v61, v66
	v_add_f32_e32 v2, v69, v2
	v_exp_f32_e32 v51, v3
	v_sub_f32_e32 v3, v62, v66
	v_add_f32_e32 v2, v38, v2
	v_exp_f32_e32 v52, v3
	v_sub_f32_e32 v3, v63, v66
	v_add_f32_e32 v2, v44, v2
	v_exp_f32_e32 v57, v3
	v_sub_f32_e32 v3, v64, v66
	v_add_f32_e32 v2, v45, v2
	v_exp_f32_e32 v58, v3
	v_sub_f32_e32 v3, v65, v66
	v_add_f32_e32 v2, v51, v2
	v_exp_f32_e32 v62, v3
	v_sub_f32_e32 v3, v82, v66
	v_add_f32_e32 v2, v52, v2
	v_exp_f32_e32 v37, v3
	v_sub_f32_e32 v3, v83, v66
	v_add_f32_e32 v2, v57, v2
	v_exp_f32_e32 v42, v3
	v_sub_f32_e32 v3, v84, v66
	v_add_f32_e32 v2, v58, v2
	v_exp_f32_e32 v43, v3
	v_sub_f32_e32 v3, v85, v66
	v_add_f32_e32 v2, v62, v2
	v_exp_f32_e32 v49, v3
	v_sub_f32_e32 v3, v86, v66
	v_add_f32_e32 v2, v37, v2
	v_exp_f32_e32 v50, v3
	v_sub_f32_e32 v3, v87, v66
	v_add_f32_e32 v2, v42, v2
	v_exp_f32_e32 v55, v3
	v_sub_f32_e32 v3, v88, v66
	v_add_f32_e32 v2, v43, v2
	v_exp_f32_e32 v56, v3
	v_sub_f32_e32 v3, v89, v66
	v_add_f32_e32 v2, v49, v2
	v_exp_f32_e32 v61, v3
	v_sub_f32_e32 v3, v90, v66
	v_add_f32_e32 v2, v50, v2
	v_exp_f32_e32 v36, v3
	v_sub_f32_e32 v3, v91, v66
	v_add_f32_e32 v2, v55, v2
	v_exp_f32_e32 v39, v3
	v_sub_f32_e32 v3, v92, v66
	v_add_f32_e32 v2, v56, v2
	v_exp_f32_e32 v40, v3
	v_add_f32_e32 v2, v61, v2
	v_add_f32_e32 v2, v36, v2
	v_add_f32_e32 v2, v39, v2
	v_add_f32_e32 v14, v40, v2
	v_sub_f32_e32 v2, v93, v66
	v_exp_f32_e32 v48, v2
	v_cvt_pk_bf16_f32 v2, v33, v18
	v_cvt_pk_bf16_f32 v3, v19, v20
	v_cvt_pk_bf16_f32 v4, v21, v22
	v_cvt_pk_bf16_f32 v5, v23, v24
	s_bitcmp1_b32 s96, 0
	s_cbranch_scc1 .Latt_b3m
	s_waitcnt vmcnt(0)
.Latt_b3m:
	s_waitcnt vmcnt(12)
	s_barrier
	ds_read_b64_tr_b16 v[10:11], v195
	ds_read_b64_tr_b16 v[12:13], v195 offset:1024
	ds_read_b64_tr_b16 v[6:7], v196
	ds_read_b64_tr_b16 v[8:9], v196 offset:1024
	s_waitcnt lgkmcnt(0)
	s_nop 0
	v_add_f32_e32 v34, v48, v14
	v_mfma_f32_32x32x16_bf16 v[18:33], v[10:13], v[2:5], 0
	v_sub_f32_e32 v10, v94, v66
	v_exp_f32_e32 v63, v10
	v_sub_f32_e32 v10, v95, v66
	v_exp_f32_e32 v65, v10
	v_sub_f32_e32 v10, v96, v66
	v_exp_f32_e32 v64, v10
	v_sub_f32_e32 v35, v70, v66
	v_mfma_f32_32x32x16_bf16 v[2:17], v[6:9], v[2:5], 0
	v_exp_f32_e32 v70, v35
	v_add_f32_e32 v34, v63, v34
	v_cvt_pk_bf16_f32 v82, v119, v120
	v_cvt_pk_bf16_f32 v83, v121, v122
	v_cvt_pk_bf16_f32 v84, v123, v124
	v_cvt_pk_bf16_f32 v85, v125, v126
	ds_read_b64_tr_b16 v[90:91], v197
	ds_read_b64_tr_b16 v[92:93], v197 offset:1024
	ds_read_b64_tr_b16 v[86:87], v198
	ds_read_b64_tr_b16 v[88:89], v198 offset:1024
	s_waitcnt lgkmcnt(0)
	v_add_f32_e32 v34, v65, v34
	v_mfma_f32_32x32x16_bf16 v[18:33], v[90:93], v[82:85], v[18:33]
	v_add_f32_e32 v34, v64, v34
	v_add_f32_e32 v59, v70, v34
	ds_bpermute_b32 v60, v118, v59
	v_mfma_f32_32x32x16_bf16 v[2:17], v[86:89], v[82:85], v[2:17]
	s_and_b64 vcc, exec, s[72:73]
	s_mov_b64 s[4:5], -1
	s_cbranch_vccnz .LBB0_473
	v_mov_b32_e32 v84, v0
	s_lshl_b32 s90, s37, 1
	v_bfe_u32 v86, v84, 3, 3
	v_or_b32_e32 v34, s2, v86
	v_mul_lo_u32 v34, v34, s81
	v_add_u32_e32 v34, s82, v34
	v_max_i32_e32 v82, 0, v34
	v_mov_b64_e32 v[34:35], s[84:85]
	v_mad_u64_u32 v[82:83], s[4:5], v82, s21, v[34:35]
	v_lshlrev_b32_e32 v84, 4, v84
	v_lshl_add_u64 v[82:83], v[82:83], 0, s[90:91]
	v_and_b32_e32 v84, 0x70, v84
	v_mov_b32_e32 v85, v179
	v_lshl_add_u64 v[82:83], v[82:83], 0, v[84:85]
	s_mov_b32 m0, s75
	v_lshl_add_u64 v[82:83], v[82:83], 0, s[94:95]
	v_or_b32_e32 v82, s10, v86
	v_mul_lo_u32 v82, v82, s81
	v_add_u32_e32 v82, s82, v82
	v_max_i32_e32 v82, 0, v82
	v_mad_u64_u32 v[82:83], s[4:5], v82, s21, v[34:35]
	v_lshl_add_u64 v[82:83], v[82:83], 0, s[90:91]
	v_lshl_add_u64 v[82:83], v[82:83], 0, v[84:85]
	v_lshl_add_u64 v[82:83], v[82:83], 0, s[94:95]
	s_mov_b32 m0, s26
	s_nop 0
	v_or_b32_e32 v82, s11, v86
	v_mul_lo_u32 v82, v82, s81
	v_add_u32_e32 v82, s82, v82
	v_max_i32_e32 v82, 0, v82
	v_mad_u64_u32 v[82:83], s[4:5], v82, s21, v[34:35]
	v_lshl_add_u64 v[82:83], v[82:83], 0, s[90:91]
	v_lshl_add_u64 v[82:83], v[82:83], 0, v[84:85]
	v_lshl_add_u64 v[82:83], v[82:83], 0, s[94:95]
	s_add_i32 m0, s75, 0x800
	s_nop 0
	v_or_b32_e32 v82, s12, v86
	v_mul_lo_u32 v82, v82, s81
	v_add_u32_e32 v82, s82, v82
	v_max_i32_e32 v82, 0, v82
	v_mad_u64_u32 v[34:35], s[4:5], v82, s21, v[34:35]
	v_lshl_add_u64 v[34:35], v[34:35], 0, s[90:91]
	v_lshl_add_u64 v[34:35], v[34:35], 0, v[84:85]
	v_lshl_add_u64 v[34:35], v[34:35], 0, s[94:95]
	s_mov_b64 s[4:5], 0
